# P5: touch the g_a/g_b cache lines one K-trip ahead of the mid-K rescale
# baseline (speedup 1.0000x reference)
; __device__ __forceinline__ void unpack8(u32x4 w, f32x4& a, f32x4& b) { a = (f32x4){bflo(w.x), bfhi(w.x), bflo(w.y), bfhi(w.y)}; b = (f32x4){bflo(w.z), bfhi(w.z), bflo(w.w), bfhi(w.w)}; }
;     __device__ __forceinline__ void mid(Acc& acc, const Unit& u, int wr, int wc, int fr, int fq) const {
;     ...
;             for (int m = 0; m < 4; ++m) { const size_t ro = (size_t)(row0 + ai * HALF + m * 16) * ldg;
; #pragma unroll
;                 for (int bj = 0; bj < 2; ++bj) { const int col = col0 + bj * HALF;
;                     f32x4 a0, a1, b0, b1; unpack8(*(const u32x4*)(GA + ro + col), a0, a1); unpack8(*(const u32x4*)(GB + ro + col), b0, b1);
; #pragma unroll
;                     for (int j = 0; j < 4; ++j) { acc[ai][bj][m][0][j] *= (1.0f + __expf(-b0[j])) * __builtin_amdgcn_rcpf(1.0f + __expf(-a0[j])); acc[ai][bj][m][1][j] *= (1.0f + __expf(-b1[j])) * __builtin_amdgcn_rcpf(1.0f + __expf(-a1[j])); } } }
; template <class Epi, class Sched, bool F8 = false, bool MID = false, bool GATHER = false>
; __device__ __forceinline__ void gemm_phase(LAS unsigned char* lds, const Gemm g, const Sched& S, const Epi& E) {
;     ...
;             if constexpr (MID) { if (t == (nt >> 1)) { if constexpr (F8) asm volatile("s_nop 15\n\ts_nop 15" ::: "memory"); int l_; asm volatile("v_mbcnt_lo_u32_b32 %0, -1, 0\n\tv_mbcnt_hi_u32_b32 %0, -1, %0" : "=v"(l_)); E.mid(acc, cur, wr, wc, l_ & 15, l_ >> 4); if constexpr (F8) asm volatile("s_nop 7" ::: "memory"); } }
.LBB0_1851:
	s_cmp_lg_u32 s86, 4
	s_cbranch_scc1 .Lp5_notouch
	v_mbcnt_lo_u32_b32 v253, -1, 0
	v_mbcnt_hi_u32_b32 v253, -1, v253
	v_lshrrev_b32_e32 v254, 1, v253
	v_add_u32_e32 v254, s78, v254
	v_mul_lo_u32 v254, v254, s73
	v_and_b32_e32 v253, 1, v253
	v_lshlrev_b32_e32 v253, 8, v253
	s_lshl_b32 s98, s77, 1
	v_add3_u32 v254, v254, v253, s98
	s_lshl_b32 s98, s73, 5
	s_lshl_b32 s99, s73, 7
	global_load_dword v253, v254, s[6:7]
	global_load_dword v253, v254, s[8:9]
	v_add_u32_e32 v255, s98, v254
	global_load_dword v253, v255, s[6:7]
	global_load_dword v253, v255, s[8:9]
	v_add_u32_e32 v254, s99, v254
	global_load_dword v253, v254, s[6:7]
	global_load_dword v253, v254, s[8:9]
	v_add_u32_e32 v255, s98, v254
	global_load_dword v253, v255, s[6:7]
	global_load_dword v253, v255, s[8:9]

; __global__ void __launch_bounds__(512, 2) mega_fwd(Args args) {
	.amdhsa_kernel _Z8mega_fwd4Args
		.amdhsa_group_segment_fixed_size 0
		.amdhsa_private_segment_fixed_size 0
		.amdhsa_kernarg_size 480
		.amdhsa_user_sgpr_count 2
		.amdhsa_user_sgpr_dispatch_ptr 0
		.amdhsa_user_sgpr_queue_ptr 0
		.amdhsa_user_sgpr_kernarg_segment_ptr 1
		.amdhsa_user_sgpr_dispatch_id 0
		.amdhsa_user_sgpr_kernarg_preload_length 0
		.amdhsa_user_sgpr_kernarg_preload_offset 0
		.amdhsa_user_sgpr_private_segment_size 0
		.amdhsa_uses_dynamic_stack 0
		.amdhsa_enable_private_segment 0
		.amdhsa_system_sgpr_workgroup_id_x 1
		.amdhsa_system_sgpr_workgroup_id_y 0
		.amdhsa_system_sgpr_workgroup_id_z 0
		.amdhsa_system_sgpr_workgroup_info 0
		.amdhsa_system_vgpr_workitem_id 0
		.amdhsa_next_free_vgpr 256
		.amdhsa_next_free_sgpr 102
		.amdhsa_accum_offset 256
		.amdhsa_reserve_vcc 1
		.amdhsa_float_round_mode_32 0
		.amdhsa_float_round_mode_16_64 0
		.amdhsa_float_denorm_mode_32 3
		.amdhsa_float_denorm_mode_16_64 3
		.amdhsa_dx10_clamp 1
		.amdhsa_ieee_mode 1
		.amdhsa_fp16_overflow 0
		.amdhsa_tg_split 0
		.amdhsa_exception_fp_ieee_invalid_op 0
		.amdhsa_exception_fp_denorm_src 0
		.amdhsa_exception_fp_ieee_div_zero 0
		.amdhsa_exception_fp_ieee_overflow 0
		.amdhsa_exception_fp_ieee_underflow 0
		.amdhsa_exception_fp_ieee_inexact 0
		.amdhsa_exception_int_div_zero 0
	.end_amdhsa_kernel

; __global__ void __launch_bounds__(512, 2) mega_fwd(Args args) {
amdhsa.kernels:
  - .agpr_count:     0
    .args:
      - .offset:         0
        .size:           224
        .value_kind:     by_value
      - .offset:         224
        .size:           4
        .value_kind:     hidden_block_count_x
      - .offset:         228
        .size:           4
        .value_kind:     hidden_block_count_y
      - .offset:         232
        .size:           4
        .value_kind:     hidden_block_count_z
      - .offset:         236
        .size:           2
        .value_kind:     hidden_group_size_x
      - .offset:         238
        .size:           2
        .value_kind:     hidden_group_size_y
      - .offset:         240
        .size:           2
        .value_kind:     hidden_group_size_z
      - .offset:         242
        .size:           2
        .value_kind:     hidden_remainder_x
      - .offset:         244
        .size:           2
        .value_kind:     hidden_remainder_y
      - .offset:         246
        .size:           2
        .value_kind:     hidden_remainder_z
      - .offset:         264
        .size:           8
        .value_kind:     hidden_global_offset_x
      - .offset:         272
        .size:           8
        .value_kind:     hidden_global_offset_y
      - .offset:         280
        .size:           8
        .value_kind:     hidden_global_offset_z
      - .offset:         288
        .size:           2
        .value_kind:     hidden_grid_dims
      - .offset:         344
        .size:           4
        .value_kind:     hidden_dynamic_lds_size
    .group_segment_fixed_size: 0
    .kernarg_segment_align: 8
    .kernarg_segment_size: 480
    .language:       OpenCL C
    .language_version:
      - 2
      - 0
    .max_flat_workgroup_size: 512
    .name:           _Z8mega_fwd4Args
    .private_segment_fixed_size: 0
    .sgpr_count:     108
    .sgpr_spill_count: 6
    .symbol:         _Z8mega_fwd4Args.kd
    .uniform_work_group_size: 1
    .uses_dynamic_stack: false
    .vgpr_count:     256
    .vgpr_spill_count: 0
    .wavefront_size: 64
